# speedup vs baseline: 1.0044x; 1.0030x over previous
.LBB1_3:
	ds_read_b128 v[128:131], v126 offset:49152
	ds_read_b128 v[132:135], v126 offset:50176
	ds_read_b128 v[136:139], v126 offset:51200
	ds_read_b128 v[140:143], v126 offset:52224
	s_add_u32 s30, s16, s0
	s_addc_u32 s31, s17, s1
	ds_read_b128 v[144:147], v110
	ds_read_b128 v[148:151], v110 offset:1024
	ds_read_b128 v[152:155], v109
	ds_read_b128 v[156:159], v109 offset:1024
	ds_read_b128 v[160:163], v108
	ds_read_b128 v[164:167], v108 offset:1024
	v_readfirstlane_b32 s34, v127
	s_mov_b32 m0, s34
	s_add_u32 s52, s30, s18
	s_addc_u32 s53, s31, s19
	global_load_lds_dwordx4 v100, s[52:53]
	v_readfirstlane_b32 s34, v125
	s_mov_b32 m0, s34
	s_nop 0
	global_load_lds_dwordx4 v101, s[52:53]
	s_waitcnt lgkmcnt(6)
	s_barrier
	s_waitcnt lgkmcnt(0)
	s_setprio 0
	s_waitcnt lgkmcnt(0)
	v_mfma_f32_16x16x32_f16 v[94:97], v[144:147], v[128:131], v[94:97]
	v_mfma_f32_16x16x32_f16 v[90:93], v[144:147], v[136:139], v[90:93]
	v_mfma_f32_16x16x32_f16 v[86:89], v[152:155], v[128:131], v[86:89]
	v_mfma_f32_16x16x32_f16 v[82:85], v[152:155], v[136:139], v[82:85]
	v_mfma_f32_16x16x32_f16 v[78:81], v[160:163], v[128:131], v[78:81]
	v_mfma_f32_16x16x32_f16 v[74:77], v[160:163], v[136:139], v[74:77]
	v_mfma_f32_16x16x32_f16 v[94:97], v[148:151], v[132:135], v[94:97]
	v_mfma_f32_16x16x32_f16 v[90:93], v[148:151], v[140:143], v[90:93]
	v_mfma_f32_16x16x32_f16 v[86:89], v[156:159], v[132:135], v[86:89]
	v_mfma_f32_16x16x32_f16 v[82:85], v[156:159], v[140:143], v[82:85]
	v_mfma_f32_16x16x32_f16 v[78:81], v[164:167], v[132:135], v[78:81]
	v_mfma_f32_16x16x32_f16 v[74:77], v[164:167], v[140:143], v[74:77]
	s_setprio 1
	s_barrier
	s_add_u32 s34, s2, s0
	s_addc_u32 s35, s3, s1
	ds_read_b128 v[168:171], v122
	ds_read_b128 v[172:175], v122 offset:1024
	ds_read_b128 v[176:179], v122 offset:2048
	ds_read_b128 v[180:183], v122 offset:3072
	v_readfirstlane_b32 s42, v106
	s_mov_b32 m0, s42
	s_add_u32 s54, s34, s20
	s_addc_u32 s55, s35, s21
	global_load_lds_dwordx4 v100, s[54:55]
	v_readfirstlane_b32 s42, v107
	s_mov_b32 m0, s42
	s_nop 0
	global_load_lds_dwordx4 v103, s[54:55]
	s_barrier
	s_waitcnt lgkmcnt(0)
	s_setprio 0
	s_waitcnt lgkmcnt(0)
	v_mfma_f32_16x16x32_f16 v[70:73], v[144:147], v[168:171], v[70:73]
	v_mfma_f32_16x16x32_f16 v[66:69], v[144:147], v[176:179], v[66:69]
	v_mfma_f32_16x16x32_f16 v[62:65], v[152:155], v[168:171], v[62:65]
	v_mfma_f32_16x16x32_f16 v[50:53], v[152:155], v[176:179], v[50:53]
	v_mfma_f32_16x16x32_f16 v[46:49], v[160:163], v[168:171], v[46:49]
	v_mfma_f32_16x16x32_f16 v[42:45], v[160:163], v[176:179], v[42:45]
	v_mfma_f32_16x16x32_f16 v[70:73], v[148:151], v[172:175], v[70:73]
	v_mfma_f32_16x16x32_f16 v[66:69], v[148:151], v[180:183], v[66:69]
	v_mfma_f32_16x16x32_f16 v[62:65], v[156:159], v[172:175], v[62:65]
	v_mfma_f32_16x16x32_f16 v[50:53], v[156:159], v[180:183], v[50:53]
	v_mfma_f32_16x16x32_f16 v[46:49], v[164:167], v[172:175], v[46:49]
	v_mfma_f32_16x16x32_f16 v[42:45], v[164:167], v[180:183], v[42:45]
	s_setprio 1
	s_barrier
	ds_read_b128 v[144:147], v110 offset:12288
	ds_read_b128 v[148:151], v110 offset:13312
	ds_read_b128 v[152:155], v109 offset:12288
	ds_read_b128 v[156:159], v109 offset:13312
	ds_read_b128 v[160:163], v108 offset:12288
	ds_read_b128 v[164:167], v108 offset:13312
	v_readfirstlane_b32 s42, v1
	s_mov_b32 m0, s42
	s_add_u32 s54, s30, s20
	s_addc_u32 s55, s31, s21
	global_load_lds_dwordx4 v100, s[54:55]
	v_readfirstlane_b32 s42, v111
	s_mov_b32 m0, s42
	s_nop 0
	global_load_lds_dwordx4 v101, s[54:55]
	s_barrier
	s_waitcnt lgkmcnt(0)
	s_setprio 0
	s_waitcnt lgkmcnt(0)
	v_mfma_f32_16x16x32_f16 v[38:41], v[144:147], v[128:131], v[38:41]
	v_mfma_f32_16x16x32_f16 v[34:37], v[144:147], v[136:139], v[34:37]
	v_mfma_f32_16x16x32_f16 v[30:33], v[152:155], v[128:131], v[30:33]
	v_mfma_f32_16x16x32_f16 v[26:29], v[152:155], v[136:139], v[26:29]
	v_mfma_f32_16x16x32_f16 v[22:25], v[160:163], v[128:131], v[22:25]
	v_mfma_f32_16x16x32_f16 v[18:21], v[160:163], v[136:139], v[18:21]
	v_mfma_f32_16x16x32_f16 v[38:41], v[148:151], v[132:135], v[38:41]
	v_mfma_f32_16x16x32_f16 v[34:37], v[148:151], v[140:143], v[34:37]
	v_mfma_f32_16x16x32_f16 v[30:33], v[156:159], v[132:135], v[30:33]
	v_mfma_f32_16x16x32_f16 v[26:29], v[156:159], v[140:143], v[26:29]
	v_mfma_f32_16x16x32_f16 v[22:25], v[164:167], v[132:135], v[22:25]
	v_mfma_f32_16x16x32_f16 v[18:21], v[164:167], v[140:143], v[18:21]
	s_setprio 1
	s_barrier
	v_readfirstlane_b32 s42, v112
	s_mov_b32 m0, s42
	s_add_u32 s56, s34, s22
	s_addc_u32 s57, s35, s23
	global_load_lds_dwordx4 v100, s[56:57]
	v_readfirstlane_b32 s42, v113
	s_mov_b32 m0, s42
	s_nop 0
	global_load_lds_dwordx4 v103, s[56:57]
	s_waitcnt vmcnt(6)
	s_barrier
	s_setprio 0
	v_mfma_f32_16x16x32_f16 v[14:17], v[144:147], v[168:171], v[14:17]
	v_mfma_f32_16x16x32_f16 v[10:13], v[144:147], v[176:179], v[10:13]
	v_mfma_f32_16x16x32_f16 v[6:9], v[152:155], v[168:171], v[6:9]
	v_mfma_f32_16x16x32_f16 v[2:5], v[152:155], v[176:179], v[2:5]
	v_mfma_f32_16x16x32_f16 v[54:57], v[160:163], v[168:171], v[54:57]
	v_mfma_f32_16x16x32_f16 v[58:61], v[160:163], v[176:179], v[58:61]
	v_mfma_f32_16x16x32_f16 v[14:17], v[148:151], v[172:175], v[14:17]
	v_mfma_f32_16x16x32_f16 v[10:13], v[148:151], v[180:183], v[10:13]
	v_mfma_f32_16x16x32_f16 v[6:9], v[156:159], v[172:175], v[6:9]
	v_mfma_f32_16x16x32_f16 v[2:5], v[156:159], v[180:183], v[2:5]
	v_mfma_f32_16x16x32_f16 v[54:57], v[164:167], v[172:175], v[54:57]
	v_mfma_f32_16x16x32_f16 v[58:61], v[164:167], v[180:183], v[58:61]
	s_setprio 1
	s_barrier
	ds_read_b128 v[128:131], v117
	ds_read_b128 v[132:135], v117 offset:1024
	ds_read_b128 v[136:139], v117 offset:2048
	ds_read_b128 v[140:143], v117 offset:3072
	ds_read_b128 v[144:147], v110 offset:24576
	ds_read_b128 v[148:151], v110 offset:25600
	ds_read_b128 v[152:155], v109 offset:24576
	ds_read_b128 v[156:159], v109 offset:25600
	ds_read_b128 v[160:163], v108 offset:24576
	ds_read_b128 v[164:167], v108 offset:25600
	v_readfirstlane_b32 s42, v115
	s_mov_b32 m0, s42
	s_add_u32 s52, s30, s24
	s_addc_u32 s53, s31, s25
	global_load_lds_dwordx4 v100, s[52:53]
	v_readfirstlane_b32 s42, v116
	s_mov_b32 m0, s42
	s_nop 0
	global_load_lds_dwordx4 v101, s[52:53]
	s_waitcnt lgkmcnt(6)
	s_barrier
	s_waitcnt lgkmcnt(0)
	s_setprio 0
	s_waitcnt lgkmcnt(0)
	v_mfma_f32_16x16x32_f16 v[94:97], v[144:147], v[128:131], v[94:97]
	v_mfma_f32_16x16x32_f16 v[90:93], v[144:147], v[136:139], v[90:93]
	v_mfma_f32_16x16x32_f16 v[86:89], v[152:155], v[128:131], v[86:89]
	v_mfma_f32_16x16x32_f16 v[82:85], v[152:155], v[136:139], v[82:85]
	v_mfma_f32_16x16x32_f16 v[78:81], v[160:163], v[128:131], v[78:81]
	v_mfma_f32_16x16x32_f16 v[74:77], v[160:163], v[136:139], v[74:77]
	v_mfma_f32_16x16x32_f16 v[94:97], v[148:151], v[132:135], v[94:97]
	v_mfma_f32_16x16x32_f16 v[90:93], v[148:151], v[140:143], v[90:93]
	v_mfma_f32_16x16x32_f16 v[86:89], v[156:159], v[132:135], v[86:89]
	v_mfma_f32_16x16x32_f16 v[82:85], v[156:159], v[140:143], v[82:85]
	v_mfma_f32_16x16x32_f16 v[78:81], v[164:167], v[132:135], v[78:81]
	v_mfma_f32_16x16x32_f16 v[74:77], v[164:167], v[140:143], v[74:77]
	s_setprio 1
	s_barrier
	ds_read_b128 v[168:171], v114
	ds_read_b128 v[172:175], v114 offset:1024
	ds_read_b128 v[176:179], v114 offset:2048
	ds_read_b128 v[180:183], v114 offset:3072
	v_readfirstlane_b32 s42, v118
	s_mov_b32 m0, s42
	s_add_u32 s54, s34, s26
	s_addc_u32 s55, s35, s27
	global_load_lds_dwordx4 v100, s[54:55]
	v_readfirstlane_b32 s42, v119
	s_mov_b32 m0, s42
	s_nop 0
	global_load_lds_dwordx4 v103, s[54:55]
	s_barrier
	s_waitcnt lgkmcnt(0)
	s_setprio 0
	s_waitcnt lgkmcnt(0)
	v_mfma_f32_16x16x32_f16 v[70:73], v[144:147], v[168:171], v[70:73]
	v_mfma_f32_16x16x32_f16 v[66:69], v[144:147], v[176:179], v[66:69]
	v_mfma_f32_16x16x32_f16 v[62:65], v[152:155], v[168:171], v[62:65]
	v_mfma_f32_16x16x32_f16 v[50:53], v[152:155], v[176:179], v[50:53]
	v_mfma_f32_16x16x32_f16 v[46:49], v[160:163], v[168:171], v[46:49]
	v_mfma_f32_16x16x32_f16 v[42:45], v[160:163], v[176:179], v[42:45]
	v_mfma_f32_16x16x32_f16 v[70:73], v[148:151], v[172:175], v[70:73]
	v_mfma_f32_16x16x32_f16 v[66:69], v[148:151], v[180:183], v[66:69]
	v_mfma_f32_16x16x32_f16 v[62:65], v[156:159], v[172:175], v[62:65]
	v_mfma_f32_16x16x32_f16 v[50:53], v[156:159], v[180:183], v[50:53]
	v_mfma_f32_16x16x32_f16 v[46:49], v[164:167], v[172:175], v[46:49]
	v_mfma_f32_16x16x32_f16 v[42:45], v[164:167], v[180:183], v[42:45]
	s_setprio 1
	s_barrier
	ds_read_b128 v[144:147], v110 offset:36864
	ds_read_b128 v[148:151], v110 offset:37888
	ds_read_b128 v[152:155], v109 offset:36864
	ds_read_b128 v[156:159], v109 offset:37888
	ds_read_b128 v[160:163], v108 offset:36864
	ds_read_b128 v[164:167], v108 offset:37888
	v_readfirstlane_b32 s42, v120
	s_mov_b32 m0, s42
	s_add_u32 s54, s30, s26
	s_addc_u32 s55, s31, s27
	global_load_lds_dwordx4 v100, s[54:55]
	s_nop 0
	v_readfirstlane_b32 s30, v121
	s_mov_b32 m0, s30
	s_nop 0
	global_load_lds_dwordx4 v101, s[54:55]
	s_barrier
	s_waitcnt lgkmcnt(0)
	s_setprio 0
	s_waitcnt lgkmcnt(0)
	v_mfma_f32_16x16x32_f16 v[38:41], v[144:147], v[128:131], v[38:41]
	v_mfma_f32_16x16x32_f16 v[34:37], v[144:147], v[136:139], v[34:37]
	v_mfma_f32_16x16x32_f16 v[30:33], v[152:155], v[128:131], v[30:33]
	v_mfma_f32_16x16x32_f16 v[26:29], v[152:155], v[136:139], v[26:29]
	v_mfma_f32_16x16x32_f16 v[22:25], v[160:163], v[128:131], v[22:25]
	v_mfma_f32_16x16x32_f16 v[18:21], v[160:163], v[136:139], v[18:21]
	v_mfma_f32_16x16x32_f16 v[38:41], v[148:151], v[132:135], v[38:41]
	v_mfma_f32_16x16x32_f16 v[34:37], v[148:151], v[140:143], v[34:37]
	v_mfma_f32_16x16x32_f16 v[30:33], v[156:159], v[132:135], v[30:33]
	v_mfma_f32_16x16x32_f16 v[26:29], v[156:159], v[140:143], v[26:29]
	v_mfma_f32_16x16x32_f16 v[22:25], v[164:167], v[132:135], v[22:25]
	v_mfma_f32_16x16x32_f16 v[18:21], v[164:167], v[140:143], v[18:21]
	s_setprio 1
	s_barrier
	v_readfirstlane_b32 s30, v123
	s_mov_b32 m0, s30
	s_add_u32 s56, s34, s28
	s_addc_u32 s57, s35, s29
	global_load_lds_dwordx4 v100, s[56:57]
	v_readfirstlane_b32 s30, v124
	s_mov_b32 m0, s30
	s_nop 0
	global_load_lds_dwordx4 v103, s[56:57]
	s_waitcnt vmcnt(6)
	s_barrier
	s_setprio 0
	v_mfma_f32_16x16x32_f16 v[14:17], v[144:147], v[168:171], v[14:17]
	v_mfma_f32_16x16x32_f16 v[10:13], v[144:147], v[176:179], v[10:13]
	v_mfma_f32_16x16x32_f16 v[6:9], v[152:155], v[168:171], v[6:9]
	v_mfma_f32_16x16x32_f16 v[2:5], v[152:155], v[176:179], v[2:5]
	v_mfma_f32_16x16x32_f16 v[54:57], v[160:163], v[168:171], v[54:57]
	v_mfma_f32_16x16x32_f16 v[58:61], v[160:163], v[176:179], v[58:61]
	v_mfma_f32_16x16x32_f16 v[14:17], v[148:151], v[172:175], v[14:17]
	v_mfma_f32_16x16x32_f16 v[10:13], v[148:151], v[180:183], v[10:13]
	v_mfma_f32_16x16x32_f16 v[6:9], v[156:159], v[172:175], v[6:9]
	v_mfma_f32_16x16x32_f16 v[2:5], v[156:159], v[180:183], v[2:5]
	v_mfma_f32_16x16x32_f16 v[54:57], v[164:167], v[172:175], v[54:57]
	v_mfma_f32_16x16x32_f16 v[58:61], v[164:167], v[180:183], v[58:61]
	s_setprio 1
	s_add_i32 s41, s41, 2
	s_add_u32 s0, s0, 0x100
	s_addc_u32 s1, s1, 0
	s_cmp_lt_u32 s41, 12
	s_barrier
	s_cbranch_scc1 .LBB1_3
	v_add_u32_e32 v98, 0x9000, v1
	s_add_u32 s0, s16, 0x30780
	v_readfirstlane_b32 s2, v98
	s_addc_u32 s1, s17, 0
	s_mov_b32 m0, s2
	v_readfirstlane_b32 s2, v125
	ds_read_b128 v[118:121], v126 offset:49152
	ds_read_b128 v[128:131], v126 offset:50176
	ds_read_b128 v[132:135], v126 offset:51200
	ds_read_b128 v[136:139], v126 offset:52224
	ds_read_b128 v[140:143], v110
	ds_read_b128 v[144:147], v110 offset:1024
	ds_read_b128 v[148:151], v109
	ds_read_b128 v[152:155], v109 offset:1024
	ds_read_b128 v[156:159], v108
	ds_read_b128 v[160:163], v108 offset:1024
	s_nop 0
	global_load_lds_dwordx4 v100, s[0:1]
	s_mov_b32 m0, s2
	s_nop 0
	global_load_lds_dwordx4 v101, s[0:1]
	s_barrier
	s_waitcnt lgkmcnt(0)
	s_setprio 0
	s_waitcnt lgkmcnt(0)
	v_mfma_f32_16x16x32_f16 v[90:93], v[140:143], v[132:135], v[90:93]
	v_mfma_f32_16x16x32_f16 v[86:89], v[148:151], v[118:121], v[86:89]
	v_mfma_f32_16x16x32_f16 v[82:85], v[148:151], v[132:135], v[82:85]
	v_mfma_f32_16x16x32_f16 v[94:97], v[140:143], v[118:121], v[94:97]
	v_mfma_f32_16x16x32_f16 v[90:93], v[144:147], v[136:139], v[90:93]
	v_mfma_f32_16x16x32_f16 v[86:89], v[152:155], v[128:131], v[86:89]
	v_mfma_f32_16x16x32_f16 v[82:85], v[152:155], v[136:139], v[82:85]
	v_mfma_f32_16x16x32_f16 v[78:81], v[156:159], v[118:121], v[78:81]
	v_mfma_f32_16x16x32_f16 v[74:77], v[156:159], v[132:135], v[74:77]
	v_mfma_f32_16x16x32_f16 v[94:97], v[144:147], v[128:131], v[94:97]
	v_mfma_f32_16x16x32_f16 v[124:127], v[160:163], v[128:131], v[78:81]
	v_mfma_f32_16x16x32_f16 v[164:167], v[160:163], v[136:139], v[74:77]
	s_setprio 1
	s_barrier
	s_nop 2
	ds_read_b128 v[74:77], v122
	ds_read_b128 v[78:81], v122 offset:1024
	ds_read_b128 v[98:101], v122 offset:2048
	ds_read_b128 v[168:171], v122 offset:3072
	s_barrier
	s_waitcnt lgkmcnt(0)
	s_setprio 0
	s_waitcnt lgkmcnt(0)
	v_mfma_f32_16x16x32_f16 v[70:73], v[140:143], v[74:77], v[70:73]
	v_mfma_f32_16x16x32_f16 v[66:69], v[140:143], v[98:101], v[66:69]
	v_mfma_f32_16x16x32_f16 v[50:53], v[148:151], v[98:101], v[50:53]
	v_mfma_f32_16x16x32_f16 v[46:49], v[156:159], v[74:77], v[46:49]
	v_mfma_f32_16x16x32_f16 v[42:45], v[156:159], v[98:101], v[42:45]
	v_mfma_f32_16x16x32_f16 v[70:73], v[144:147], v[78:81], v[70:73]
	v_mfma_f32_16x16x32_f16 v[66:69], v[144:147], v[168:171], v[66:69]
	v_mfma_f32_16x16x32_f16 v[62:65], v[148:151], v[74:77], v[62:65]
	v_mfma_f32_16x16x32_f16 v[50:53], v[152:155], v[168:171], v[50:53]
	v_mfma_f32_16x16x32_f16 v[46:49], v[160:163], v[78:81], v[46:49]
	v_mfma_f32_16x16x32_f16 v[42:45], v[160:163], v[168:171], v[42:45]
	v_mfma_f32_16x16x32_f16 v[140:143], v[152:155], v[78:81], v[62:65]
	s_setprio 1
	s_barrier
	s_nop 1
	ds_read_b128 v[62:65], v110 offset:12288
	ds_read_b128 v[144:147], v110 offset:13312
	ds_read_b128 v[148:151], v109 offset:12288
	ds_read_b128 v[152:155], v109 offset:13312
	ds_read_b128 v[156:159], v108 offset:12288
	ds_read_b128 v[160:163], v108 offset:13312
	s_waitcnt vmcnt(4)
	s_barrier
	s_waitcnt lgkmcnt(0)
	s_setprio 0
	s_waitcnt lgkmcnt(0)
	v_mfma_f32_16x16x32_f16 v[38:41], v[62:65], v[118:121], v[38:41]
	v_mfma_f32_16x16x32_f16 v[34:37], v[62:65], v[132:135], v[34:37]
	v_mfma_f32_16x16x32_f16 v[30:33], v[148:151], v[118:121], v[30:33]
	v_mfma_f32_16x16x32_f16 v[26:29], v[148:151], v[132:135], v[26:29]
	v_mfma_f32_16x16x32_f16 v[22:25], v[156:159], v[118:121], v[22:25]
	v_mfma_f32_16x16x32_f16 v[18:21], v[156:159], v[132:135], v[18:21]
	v_mfma_f32_16x16x32_f16 v[38:41], v[144:147], v[128:131], v[38:41]
	v_mfma_f32_16x16x32_f16 v[34:37], v[144:147], v[136:139], v[34:37]
	v_mfma_f32_16x16x32_f16 v[30:33], v[152:155], v[128:131], v[30:33]
	v_mfma_f32_16x16x32_f16 v[26:29], v[152:155], v[136:139], v[26:29]
	v_mfma_f32_16x16x32_f16 v[22:25], v[160:163], v[128:131], v[22:25]
	v_mfma_f32_16x16x32_f16 v[18:21], v[160:163], v[136:139], v[18:21]
	s_setprio 1
	s_setprio 0
	v_mfma_f32_16x16x32_f16 v[10:13], v[62:65], v[98:101], v[10:13]
	v_mfma_f32_16x16x32_f16 v[128:131], v[144:147], v[168:171], v[10:13]
	v_mfma_f32_16x16x32_f16 v[6:9], v[148:151], v[74:77], v[6:9]
	v_mfma_f32_16x16x32_f16 v[2:5], v[148:151], v[98:101], v[2:5]
	v_mfma_f32_16x16x32_f16 v[10:13], v[156:159], v[74:77], v[54:57]
	v_mfma_f32_16x16x32_f16 v[14:17], v[62:65], v[74:77], v[14:17]
	v_mfma_f32_16x16x32_f16 v[6:9], v[152:155], v[78:81], v[6:9]
	v_mfma_f32_16x16x32_f16 v[2:5], v[152:155], v[168:171], v[2:5]
	v_mfma_f32_16x16x32_f16 v[132:135], v[160:163], v[78:81], v[10:13]
	v_mfma_f32_16x16x32_f16 v[10:13], v[156:159], v[98:101], v[58:61]
	v_mfma_f32_16x16x32_f16 v[118:121], v[144:147], v[78:81], v[14:17]
	v_mfma_f32_16x16x32_f16 v[136:139], v[160:163], v[168:171], v[10:13]
	s_setprio 1
	s_barrier
	s_nop 3
	ds_read_b128 v[10:13], v117
	ds_read_b128 v[14:17], v117 offset:1024
	ds_read_b128 v[144:147], v117 offset:2048
	ds_read_b128 v[148:151], v117 offset:3072
	ds_read_b128 v[54:57], v110 offset:24576
	ds_read_b128 v[152:155], v110 offset:25600
	ds_read_b128 v[156:159], v109 offset:24576
	ds_read_b128 v[160:163], v109 offset:25600
	ds_read_b128 v[168:171], v108 offset:24576
	ds_read_b128 v[172:175], v108 offset:25600
	s_waitcnt vmcnt(2)
	s_barrier
	s_waitcnt lgkmcnt(0)
	s_setprio 0
	s_waitcnt lgkmcnt(0)
	v_mfma_f32_16x16x32_f16 v[58:61], v[54:57], v[10:13], v[94:97]
	v_mfma_f32_16x16x32_f16 v[98:101], v[152:155], v[14:17], v[58:61]
	v_mfma_f32_16x16x32_f16 v[58:61], v[54:57], v[144:147], v[90:93]
	v_mfma_f32_16x16x32_f16 v[90:93], v[152:155], v[148:151], v[58:61]
	v_mfma_f32_16x16x32_f16 v[58:61], v[156:159], v[10:13], v[86:89]
	v_mfma_f32_16x16x32_f16 v[78:81], v[160:163], v[14:17], v[58:61]
	v_mfma_f32_16x16x32_f16 v[58:61], v[156:159], v[144:147], v[82:85]
	v_mfma_f32_16x16x32_f16 v[74:77], v[160:163], v[148:151], v[58:61]
	v_mfma_f32_16x16x32_f16 v[58:61], v[168:171], v[10:13], v[124:127]
	v_mfma_f32_16x16x32_f16 v[62:65], v[172:175], v[14:17], v[58:61]
	v_mfma_f32_16x16x32_f16 v[58:61], v[168:171], v[144:147], v[164:167]
	v_mfma_f32_16x16x32_f16 v[58:61], v[172:175], v[148:151], v[58:61]
	s_setprio 1
	s_barrier
	ds_read_b128 v[94:97], v114
	ds_read_b128 v[122:125], v114 offset:1024
	ds_read_b128 v[164:167], v114 offset:2048
	ds_read_b128 v[112:115], v114 offset:3072
	s_waitcnt vmcnt(0)
	s_barrier
	s_waitcnt lgkmcnt(0)
	s_setprio 0
	s_waitcnt lgkmcnt(0)
	v_mfma_f32_16x16x32_f16 v[70:73], v[54:57], v[94:97], v[70:73]
	v_mfma_f32_16x16x32_f16 v[54:57], v[54:57], v[164:167], v[66:69]
	v_mfma_f32_16x16x32_f16 v[82:85], v[152:155], v[112:115], v[54:57]
	v_mfma_f32_16x16x32_f16 v[54:57], v[156:159], v[94:97], v[140:143]
	v_mfma_f32_16x16x32_f16 v[50:53], v[156:159], v[164:167], v[50:53]
	v_mfma_f32_16x16x32_f16 v[46:49], v[168:171], v[94:97], v[46:49]
	v_mfma_f32_16x16x32_f16 v[42:45], v[168:171], v[164:167], v[42:45]
	v_mfma_f32_16x16x32_f16 v[86:89], v[152:155], v[122:125], v[70:73]
	v_mfma_f32_16x16x32_f16 v[70:73], v[160:163], v[122:125], v[54:57]
	v_mfma_f32_16x16x32_f16 v[66:69], v[160:163], v[112:115], v[50:53]
	v_mfma_f32_16x16x32_f16 v[54:57], v[172:175], v[122:125], v[46:49]
	v_mfma_f32_16x16x32_f16 v[50:53], v[172:175], v[112:115], v[42:45]
	s_setprio 1
	s_barrier
	ds_read_b128 v[140:143], v110 offset:36864
	ds_read_b128 v[152:155], v110 offset:37888
	ds_read_b128 v[156:159], v109 offset:36864
	ds_read_b128 v[160:163], v109 offset:37888
	ds_read_b128 v[168:171], v108 offset:36864
	ds_read_b128 v[106:109], v108 offset:37888
	s_barrier
	s_waitcnt lgkmcnt(0)
	s_setprio 0
	s_waitcnt lgkmcnt(0)
	v_mfma_f32_16x16x32_f16 v[38:41], v[140:143], v[10:13], v[38:41]
	v_mfma_f32_16x16x32_f16 v[30:33], v[156:159], v[10:13], v[30:33]
	v_mfma_f32_16x16x32_f16 v[10:13], v[168:171], v[10:13], v[22:25]
	v_mfma_f32_16x16x32_f16 v[46:49], v[152:155], v[14:17], v[38:41]
	v_mfma_f32_16x16x32_f16 v[34:37], v[140:143], v[144:147], v[34:37]
	v_mfma_f32_16x16x32_f16 v[30:33], v[160:163], v[14:17], v[30:33]
	v_mfma_f32_16x16x32_f16 v[26:29], v[156:159], v[144:147], v[26:29]
	v_mfma_f32_16x16x32_f16 v[14:17], v[106:109], v[14:17], v[10:13]
	v_mfma_f32_16x16x32_f16 v[10:13], v[168:171], v[144:147], v[18:21]
	v_mfma_f32_16x16x32_f16 v[42:45], v[152:155], v[148:151], v[34:37]
	v_mfma_f32_16x16x32_f16 v[26:29], v[160:163], v[148:151], v[26:29]
	v_mfma_f32_16x16x32_f16 v[10:13], v[106:109], v[148:151], v[10:13]
	s_setprio 1
	s_setprio 0
	v_mfma_f32_16x16x32_f16 v[18:21], v[140:143], v[94:97], v[118:121]
	v_mfma_f32_16x16x32_f16 v[38:41], v[152:155], v[122:125], v[18:21]
	v_mfma_f32_16x16x32_f16 v[18:21], v[140:143], v[164:167], v[128:131]
	v_mfma_f32_16x16x32_f16 v[2:5], v[156:159], v[164:167], v[2:5]
	v_mfma_f32_16x16x32_f16 v[34:37], v[152:155], v[112:115], v[18:21]
	v_mfma_f32_16x16x32_f16 v[6:9], v[156:159], v[94:97], v[6:9]
	v_mfma_f32_16x16x32_f16 v[18:21], v[160:163], v[112:115], v[2:5]
	v_mfma_f32_16x16x32_f16 v[2:5], v[168:171], v[94:97], v[132:135]
	v_mfma_f32_16x16x32_f16 v[22:25], v[160:163], v[122:125], v[6:9]
	v_mfma_f32_16x16x32_f16 v[6:9], v[106:109], v[122:125], v[2:5]
	v_mfma_f32_16x16x32_f16 v[2:5], v[168:171], v[164:167], v[136:139]
	v_mfma_f32_16x16x32_f16 v[2:5], v[106:109], v[112:115], v[2:5]
	s_setprio 1
	s_andn2_b64 vcc, exec, vcc
	s_barrier
	s_cbranch_vccnz .LBB1_6
	s_barrier
